# P7 out-proj epilogue: residual x loads pipelined 7 steps ahead in a VGPR ring; P3 Q row-scale loads hoisted
# baseline (speedup 1.0000x reference)
; __device__ __forceinline__ unsigned cvt_pk4_fp8(float a, float b, float c, float d) { int w; asm("" : "=v"(w));     w = __builtin_amdgcn_cvt_pk_fp8_f32(a, b, w, false); w = __builtin_amdgcn_cvt_pk_fp8_f32(c, d, w, true); return (unsigned)w; }
;     __device__ __forceinline__ void operator()(const f32x4 (&acc)[2][2][4][2], const Unit& u, int wr, int wc, int fr, int fq) const {
;         const int row0 = u.pm * BM + wr * 64 + fr, col0 = u.pn * BM + wc * 32 + 8 * fq;
; #pragma unroll
;         for (int ai = 0; ai < 2; ++ai)
; #pragma unroll
;             for (int m = 0; m < 4; ++m) { const int r = row0 + ai * HALF + m * 16; const float c = rs[r] * (1.0f / W8_SCALE);     unsigned char* rowp = O + (size_t)r * ldc + col0;
; #pragma unroll
;                 for (int bj = 0; bj < 2; ++bj) { const f32x4 v0 = acc[ai][bj][m][0] * c, v1 = acc[ai][bj][m][1] * c;
;                     u32x2 w; w.x = cvt_pk4_fp8(v0[0], v0[1], v0[2], v0[3]); w.y = cvt_pk4_fp8(v1[0], v1[1], v1[2], v1[3]);
;                     *(u32x2*)(rowp + bj * HALF) = w; } }
.LBB0_374:
	s_lshl_b32 s15, s50, 8
	s_add_i32 s15, s15, s34
	v_mbcnt_lo_u32_b32 v132, -1, 0
	v_mbcnt_hi_u32_b32 v132, -1, v132
	v_readlane_b32 s46, v252, 21
	v_and_or_b32 v128, v132, 15, s15
	v_ashrrev_i32_e32 v129, 31, v128
	v_lshl_add_u64 v[136:137], v[128:129], 2, s[6:7]
	global_load_dword v129, v[136:137], off
	global_load_dword v240, v[136:137], off offset:64
	global_load_dword v241, v[136:137], off offset:128
	global_load_dword v242, v[136:137], off offset:192
	global_load_dword v243, v[136:137], off offset:512
	global_load_dword v244, v[136:137], off offset:576
	global_load_dword v245, v[136:137], off offset:640
	global_load_dword v246, v[136:137], off offset:704
	s_lshl_b32 s15, s76, 8
	v_ashrrev_i32_e32 v132, 1, v132
	s_or_b32 s15, s15, s84
	v_and_b32_e32 v132, -8, v132
	v_add_u32_e32 v134, s15, v132
	v_mov_b32_e32 v148, v133
	v_mov_b32_e32 v149, v133
	v_mov_b32_e32 v150, v133
	v_mov_b32_e32 v151, v133
	v_readlane_b32 s47, v252, 22
	v_or_b32_e32 v154, 16, v128
	v_ashrrev_i32_e32 v135, 31, v134
	v_mov_b64_e32 v[130:131], s[46:47]
	v_mad_i64_i32 v[152:153], s[52:53], v128, s74, v[130:131]
	v_ashrrev_i32_e32 v155, 31, v154
	s_andn2_b64 vcc, exec, s[48:49]
	s_waitcnt vmcnt(0)
	v_mul_f32_e32 v132, 0x3c800000, v129
	v_pk_mul_f32 v[124:125], v[124:125], v[132:133] op_sel_hi:[1,0]
	v_pk_mul_f32 v[120:121], v[120:121], v[132:133] op_sel_hi:[1,0]
	v_pk_mul_f32 v[116:117], v[116:117], v[132:133] op_sel_hi:[1,0]
	v_pk_mul_f32 v[112:113], v[112:113], v[132:133] op_sel_hi:[1,0]
	v_cvt_pk_fp8_f32 v148, v124, v125
	v_cvt_pk_fp8_f32 v149, v120, v121
	v_cvt_pk_fp8_f32 v150, v116, v117
	v_cvt_pk_fp8_f32 v151, v112, v113
	v_pk_mul_f32 v[126:127], v[126:127], v[132:133] op_sel_hi:[1,0]
	v_pk_mul_f32 v[122:123], v[122:123], v[132:133] op_sel_hi:[1,0]
	v_pk_mul_f32 v[118:119], v[118:119], v[132:133] op_sel_hi:[1,0]
	v_pk_mul_f32 v[114:115], v[114:115], v[132:133] op_sel_hi:[1,0]
	v_cvt_pk_fp8_f32 v148, v126, v127 op_sel:[0,0,1]
	v_cvt_pk_fp8_f32 v149, v122, v123 op_sel:[0,0,1]
	v_cvt_pk_fp8_f32 v150, v118, v119 op_sel:[0,0,1]
	v_cvt_pk_fp8_f32 v151, v114, v115 op_sel:[0,0,1]
	v_lshl_add_u64 v[112:113], v[152:153], 0, v[134:135]
	v_lshl_add_u64 v[114:115], v[154:155], 2, s[6:7]
	global_store_dwordx2 v[112:113], v[148:149], off
	global_store_dwordx2 v[112:113], v[150:151], off offset:128
	v_mov_b32_e32 v120, v240
	v_mov_b32_e32 v112, v133
	v_mov_b32_e32 v113, v133
	v_mov_b32_e32 v114, v133
	v_mov_b32_e32 v115, v133
	v_or_b32_e32 v116, 32, v128
	v_mad_i64_i32 v[118:119], s[52:53], v154, s74, v[130:131]
	v_ashrrev_i32_e32 v117, 31, v116
	v_mov_b32_e32 v132, v133
	v_mul_f32_e32 v120, 0x3c800000, v120
	v_pk_mul_f32 v[108:109], v[108:109], v[120:121] op_sel_hi:[1,0]
	v_pk_mul_f32 v[104:105], v[104:105], v[120:121] op_sel_hi:[1,0]
	v_pk_mul_f32 v[100:101], v[100:101], v[120:121] op_sel_hi:[1,0]
	v_pk_mul_f32 v[96:97], v[96:97], v[120:121] op_sel_hi:[1,0]
	v_cvt_pk_fp8_f32 v112, v108, v109
	v_cvt_pk_fp8_f32 v113, v104, v105
	v_cvt_pk_fp8_f32 v114, v100, v101
	v_cvt_pk_fp8_f32 v115, v96, v97
	v_pk_mul_f32 v[110:111], v[110:111], v[120:121] op_sel_hi:[1,0]
	v_pk_mul_f32 v[106:107], v[106:107], v[120:121] op_sel_hi:[1,0]
	v_pk_mul_f32 v[102:103], v[102:103], v[120:121] op_sel_hi:[1,0]
	v_pk_mul_f32 v[98:99], v[98:99], v[120:121] op_sel_hi:[1,0]
	v_cvt_pk_fp8_f32 v112, v110, v111 op_sel:[0,0,1]
	v_cvt_pk_fp8_f32 v113, v106, v107 op_sel:[0,0,1]
	v_cvt_pk_fp8_f32 v114, v102, v103 op_sel:[0,0,1]
	v_cvt_pk_fp8_f32 v115, v98, v99 op_sel:[0,0,1]
	v_lshl_add_u64 v[96:97], v[118:119], 0, v[134:135]
	v_lshl_add_u64 v[98:99], v[116:117], 2, s[6:7]
	global_store_dwordx2 v[96:97], v[112:113], off
	global_store_dwordx2 v[96:97], v[114:115], off offset:128
	v_mov_b32_e32 v104, v241
	v_mov_b32_e32 v96, v133
	v_mov_b32_e32 v97, v133
	v_mov_b32_e32 v98, v133
	v_mov_b32_e32 v99, v133
	v_or_b32_e32 v100, 48, v128
	v_mad_i64_i32 v[102:103], s[52:53], v116, s74, v[130:131]
	v_ashrrev_i32_e32 v101, 31, v100
	v_mul_f32_e32 v104, 0x3c800000, v104
	v_pk_mul_f32 v[92:93], v[92:93], v[104:105] op_sel_hi:[1,0]
	v_pk_mul_f32 v[88:89], v[88:89], v[104:105] op_sel_hi:[1,0]
	v_pk_mul_f32 v[84:85], v[84:85], v[104:105] op_sel_hi:[1,0]
	v_pk_mul_f32 v[80:81], v[80:81], v[104:105] op_sel_hi:[1,0]
	v_cvt_pk_fp8_f32 v96, v92, v93
	v_cvt_pk_fp8_f32 v97, v88, v89
	v_cvt_pk_fp8_f32 v98, v84, v85
	v_cvt_pk_fp8_f32 v99, v80, v81
	v_pk_mul_f32 v[94:95], v[94:95], v[104:105] op_sel_hi:[1,0]
	v_pk_mul_f32 v[90:91], v[90:91], v[104:105] op_sel_hi:[1,0]
	v_pk_mul_f32 v[86:87], v[86:87], v[104:105] op_sel_hi:[1,0]
	v_pk_mul_f32 v[82:83], v[82:83], v[104:105] op_sel_hi:[1,0]
	v_cvt_pk_fp8_f32 v96, v94, v95 op_sel:[0,0,1]
	v_cvt_pk_fp8_f32 v97, v90, v91 op_sel:[0,0,1]
	v_cvt_pk_fp8_f32 v98, v86, v87 op_sel:[0,0,1]
	v_cvt_pk_fp8_f32 v99, v82, v83 op_sel:[0,0,1]
	v_lshl_add_u64 v[80:81], v[102:103], 0, v[134:135]
	v_lshl_add_u64 v[82:83], v[100:101], 2, s[6:7]
	global_store_dwordx2 v[80:81], v[96:97], off
	global_store_dwordx2 v[80:81], v[98:99], off offset:128
	v_mov_b32_e32 v84, v242
	v_mov_b32_e32 v80, v133
	v_mov_b32_e32 v81, v133
	v_mov_b32_e32 v82, v133
	v_mov_b32_e32 v83, v133
	v_mul_f32_e32 v84, 0x3c800000, v84
	v_pk_mul_f32 v[76:77], v[76:77], v[84:85] op_sel_hi:[1,0]
	v_pk_mul_f32 v[72:73], v[72:73], v[84:85] op_sel_hi:[1,0]
	v_pk_mul_f32 v[68:69], v[68:69], v[84:85] op_sel_hi:[1,0]
	v_pk_mul_f32 v[64:65], v[64:65], v[84:85] op_sel_hi:[1,0]
	v_cvt_pk_fp8_f32 v80, v76, v77
	v_cvt_pk_fp8_f32 v81, v72, v73
	v_cvt_pk_fp8_f32 v82, v68, v69
; __device__ __forceinline__ unsigned cvt_pk4_fp8(float a, float b, float c, float d) { int w; asm("" : "=v"(w));     w = __builtin_amdgcn_cvt_pk_fp8_f32(a, b, w, false); w = __builtin_amdgcn_cvt_pk_fp8_f32(c, d, w, true); return (unsigned)w; }
; #define PG8_BAR __builtin_amdgcn_s_barrier()
;     __device__ __forceinline__ void operator()(const f32x4 (&acc)[2][2][4][2], const Unit& u, int wr, int wc, int fr, int fq) const {
;     ...
;             for (int m = 0; m < 4; ++m) { const int r = row0 + ai * HALF + m * 16; const float c = rs[r] * (1.0f / W8_SCALE);     unsigned char* rowp = O + (size_t)r * ldc + col0;
; #pragma unroll
;                 for (int bj = 0; bj < 2; ++bj) { const f32x4 v0 = acc[ai][bj][m][0] * c, v1 = acc[ai][bj][m][1] * c;
;                     u32x2 w; w.x = cvt_pk4_fp8(v0[0], v0[1], v0[2], v0[3]); w.y = cvt_pk4_fp8(v1[0], v1[1], v1[2], v1[3]);
;                     *(u32x2*)(rowp + bj * HALF) = w; } }
; template <bool FP8 = false, class Epi, class Sched>
; __device__ __forceinline__ void gemm_phase(LAS unsigned char* lds, const int K, const int lda, const int ldb, const Sched& S, const Epi& E, const int wid) {
;     ...
;         if (!has_next) break;
; #pragma unroll
;         for (int a = 0; a < 2; ++a)
; #pragma unroll
;             for (int b = 0; b < 2; ++b)
; #pragma unroll
;                 for (int m = 0; m < 4; ++m)
; #pragma unroll
;                     for (int n = 0; n < 2; ++n) acc[a][b][m][n] = (f32x4){0.f, 0.f, 0.f, 0.f};
;         cur = nxt; cA = nA; cB = nB; ++ui;
;         if (wr == 1) PG8_BAR;
	v_cvt_pk_fp8_f32 v83, v64, v65
	v_pk_mul_f32 v[78:79], v[78:79], v[84:85] op_sel_hi:[1,0]
	v_pk_mul_f32 v[74:75], v[74:75], v[84:85] op_sel_hi:[1,0]
	v_pk_mul_f32 v[70:71], v[70:71], v[84:85] op_sel_hi:[1,0]
	v_pk_mul_f32 v[66:67], v[66:67], v[84:85] op_sel_hi:[1,0]
	v_cvt_pk_fp8_f32 v80, v78, v79 op_sel:[0,0,1]
	v_cvt_pk_fp8_f32 v81, v74, v75 op_sel:[0,0,1]
	v_cvt_pk_fp8_f32 v82, v70, v71 op_sel:[0,0,1]
	v_cvt_pk_fp8_f32 v83, v66, v67 op_sel:[0,0,1]
	v_mad_i64_i32 v[64:65], s[52:53], v100, s74, v[130:131]
	v_lshl_add_u64 v[64:65], v[64:65], 0, v[134:135]
	global_store_dwordx2 v[64:65], v[80:81], off
	global_store_dwordx2 v[64:65], v[82:83], off offset:128
	v_mov_b32_e32 v68, v243
	v_add_u32_e32 v69, 0x80, v128
	v_mov_b32_e32 v64, v133
	v_mov_b32_e32 v65, v133
	v_mov_b32_e32 v66, v133
	v_mov_b32_e32 v67, v133
	v_mul_f32_e32 v68, 0x3c800000, v68
	v_pk_mul_f32 v[60:61], v[60:61], v[68:69] op_sel_hi:[1,0]
	v_pk_mul_f32 v[56:57], v[56:57], v[68:69] op_sel_hi:[1,0]
	v_pk_mul_f32 v[52:53], v[52:53], v[68:69] op_sel_hi:[1,0]
	v_pk_mul_f32 v[48:49], v[48:49], v[68:69] op_sel_hi:[1,0]
	v_cvt_pk_fp8_f32 v64, v60, v61
	v_cvt_pk_fp8_f32 v65, v56, v57
	v_cvt_pk_fp8_f32 v66, v52, v53
	v_cvt_pk_fp8_f32 v67, v48, v49
	v_pk_mul_f32 v[62:63], v[62:63], v[68:69] op_sel_hi:[1,0]
	v_pk_mul_f32 v[58:59], v[58:59], v[68:69] op_sel_hi:[1,0]
	v_pk_mul_f32 v[54:55], v[54:55], v[68:69] op_sel_hi:[1,0]
	v_pk_mul_f32 v[50:51], v[50:51], v[68:69] op_sel_hi:[1,0]
	v_cvt_pk_fp8_f32 v64, v62, v63 op_sel:[0,0,1]
	v_cvt_pk_fp8_f32 v65, v58, v59 op_sel:[0,0,1]
	v_cvt_pk_fp8_f32 v66, v54, v55 op_sel:[0,0,1]
	v_cvt_pk_fp8_f32 v67, v50, v51 op_sel:[0,0,1]
	v_mad_i64_i32 v[48:49], s[52:53], v69, s74, v[130:131]
	v_lshl_add_u64 v[48:49], v[48:49], 0, v[134:135]
	global_store_dwordx2 v[48:49], v[64:65], off
	global_store_dwordx2 v[48:49], v[66:67], off offset:128
	v_mov_b32_e32 v52, v244
	v_add_u32_e32 v53, 0x90, v128
	v_mov_b32_e32 v48, v133
	v_mov_b32_e32 v49, v133
	v_mov_b32_e32 v50, v133
	v_mov_b32_e32 v51, v133
	v_mul_f32_e32 v52, 0x3c800000, v52
	v_pk_mul_f32 v[44:45], v[44:45], v[52:53] op_sel_hi:[1,0]
	v_pk_mul_f32 v[40:41], v[40:41], v[52:53] op_sel_hi:[1,0]
	v_pk_mul_f32 v[36:37], v[36:37], v[52:53] op_sel_hi:[1,0]
	v_pk_mul_f32 v[32:33], v[32:33], v[52:53] op_sel_hi:[1,0]
	v_cvt_pk_fp8_f32 v48, v44, v45
	v_cvt_pk_fp8_f32 v49, v40, v41
	v_cvt_pk_fp8_f32 v50, v36, v37
	v_cvt_pk_fp8_f32 v51, v32, v33
	v_pk_mul_f32 v[46:47], v[46:47], v[52:53] op_sel_hi:[1,0]
	v_pk_mul_f32 v[42:43], v[42:43], v[52:53] op_sel_hi:[1,0]
	v_pk_mul_f32 v[38:39], v[38:39], v[52:53] op_sel_hi:[1,0]
	v_pk_mul_f32 v[34:35], v[34:35], v[52:53] op_sel_hi:[1,0]
	v_cvt_pk_fp8_f32 v48, v46, v47 op_sel:[0,0,1]
	v_cvt_pk_fp8_f32 v49, v42, v43 op_sel:[0,0,1]
	v_cvt_pk_fp8_f32 v50, v38, v39 op_sel:[0,0,1]
	v_cvt_pk_fp8_f32 v51, v34, v35 op_sel:[0,0,1]
	v_mad_i64_i32 v[32:33], s[52:53], v53, s74, v[130:131]
	v_lshl_add_u64 v[32:33], v[32:33], 0, v[134:135]
	global_store_dwordx2 v[32:33], v[48:49], off
	global_store_dwordx2 v[32:33], v[50:51], off offset:128
	v_mov_b32_e32 v36, v245
	v_add_u32_e32 v37, 0xa0, v128
	v_mov_b32_e32 v32, v133
	v_mov_b32_e32 v33, v133
	v_mov_b32_e32 v34, v133
	v_mov_b32_e32 v35, v133
	v_mul_f32_e32 v36, 0x3c800000, v36
	v_pk_mul_f32 v[28:29], v[28:29], v[36:37] op_sel_hi:[1,0]
	v_pk_mul_f32 v[24:25], v[24:25], v[36:37] op_sel_hi:[1,0]
	v_pk_mul_f32 v[20:21], v[20:21], v[36:37] op_sel_hi:[1,0]
	v_pk_mul_f32 v[16:17], v[16:17], v[36:37] op_sel_hi:[1,0]
	v_cvt_pk_fp8_f32 v32, v28, v29
	v_cvt_pk_fp8_f32 v33, v24, v25
	v_cvt_pk_fp8_f32 v34, v20, v21
	v_cvt_pk_fp8_f32 v35, v16, v17
	v_pk_mul_f32 v[30:31], v[30:31], v[36:37] op_sel_hi:[1,0]
	v_pk_mul_f32 v[26:27], v[26:27], v[36:37] op_sel_hi:[1,0]
	v_pk_mul_f32 v[22:23], v[22:23], v[36:37] op_sel_hi:[1,0]
	v_pk_mul_f32 v[18:19], v[18:19], v[36:37] op_sel_hi:[1,0]
	v_cvt_pk_fp8_f32 v32, v30, v31 op_sel:[0,0,1]
	v_cvt_pk_fp8_f32 v33, v26, v27 op_sel:[0,0,1]
	v_cvt_pk_fp8_f32 v34, v22, v23 op_sel:[0,0,1]
	v_cvt_pk_fp8_f32 v35, v18, v19 op_sel:[0,0,1]
	v_mad_i64_i32 v[16:17], s[52:53], v37, s74, v[130:131]
	v_lshl_add_u64 v[16:17], v[16:17], 0, v[134:135]
	global_store_dwordx2 v[16:17], v[32:33], off
	global_store_dwordx2 v[16:17], v[34:35], off offset:128
	v_mov_b32_e32 v18, v246
	v_add_u32_e32 v19, 0xb0, v128
	v_mov_b32_e32 v16, v133
	v_mov_b32_e32 v17, v133
	v_mul_f32_e32 v18, 0x3c800000, v18
	v_pk_mul_f32 v[12:13], v[12:13], v[18:19] op_sel_hi:[1,0]
	v_pk_mul_f32 v[8:9], v[8:9], v[18:19] op_sel_hi:[1,0]
	v_pk_mul_f32 v[4:5], v[4:5], v[18:19] op_sel_hi:[1,0]
	v_pk_mul_f32 v[0:1], v[0:1], v[18:19] op_sel_hi:[1,0]
	v_cvt_pk_fp8_f32 v16, v12, v13
	v_cvt_pk_fp8_f32 v17, v8, v9
	v_cvt_pk_fp8_f32 v132, v4, v5
	v_cvt_pk_fp8_f32 v133, v0, v1
	v_pk_mul_f32 v[14:15], v[14:15], v[18:19] op_sel_hi:[1,0]
	v_pk_mul_f32 v[10:11], v[10:11], v[18:19] op_sel_hi:[1,0]
	v_pk_mul_f32 v[6:7], v[6:7], v[18:19] op_sel_hi:[1,0]
	v_pk_mul_f32 v[2:3], v[2:3], v[18:19] op_sel_hi:[1,0]
	v_cvt_pk_fp8_f32 v16, v14, v15 op_sel:[0,0,1]
	v_cvt_pk_fp8_f32 v17, v10, v11 op_sel:[0,0,1]
	v_cvt_pk_fp8_f32 v132, v6, v7 op_sel:[0,0,1]
	v_cvt_pk_fp8_f32 v133, v2, v3 op_sel:[0,0,1]
	v_mad_i64_i32 v[0:1], s[48:49], v19, s74, v[130:131]
	v_lshl_add_u64 v[0:1], v[0:1], 0, v[134:135]
	s_mov_b64 s[48:49], -1
	global_store_dwordx2 v[0:1], v[16:17], off
	global_store_dwordx2 v[0:1], v[132:133], off offset:128
	s_cbranch_vccnz .LBB0_367
	s_andn2_b64 vcc, exec, s[4:5]
	s_cbranch_vccnz .LBB0_366
	s_barrier
	s_branch .LBB0_366

; __device__ __forceinline__ unsigned cvt_pk_bf16(float lo, float hi) { unsigned r; asm volatile("v_cvt_pk_bf16_f32 %0, %1, %2" : "=v"(r) : "v"(lo), "v"(hi)); return r; }
; __device__ __forceinline__ unsigned cvt_pk4_fp8(float a, float b, float c, float d) { int w; asm("" : "=v"(w));     w = __builtin_amdgcn_cvt_pk_fp8_f32(a, b, w, false); w = __builtin_amdgcn_cvt_pk_fp8_f32(c, d, w, true); return (unsigned)w; }
;     __device__ __forceinline__ void operator()(const f32x4 (&acc)[2][2][4][2], const Unit& u, int wr, int wc, int fr, int fq) const {
;         const int row0 = u.pm * BM + wr * 64 + fr, col0 = u.pn * BM + wc * 32 + 8 * fq;
;         f32x4 gv[2][2];
; #pragma unroll
;         for (int bj = 0; bj < 2; ++bj)
; #pragma unroll
;             for (int n = 0; n < 2; ++n) gv[bj][n] = *(const f32x4*)(g + col0 + bj * HALF + 4 * n);
; #pragma unroll
;         for (int ai = 0; ai < 2; ++ai)
; #pragma unroll
;             for (int m = 0; m < 4; ++m) { const size_t off = (size_t)(row0 + ai * HALF + m * 16) * DM + col0;
; #pragma unroll
;                 for (int bj = 0; bj < 2; ++bj) { const f32x4 v0 = *(const f32x4*)(base + off + bj * HALF) + acc[ai][bj][m][0], v1 = *(const f32x4*)(base + off + bj * HALF + 4) + acc[ai][bj][m][1];
;                     { u32x4 xw; xw.x = cvt_pk_bf16(v0[0], v0[1]); xw.y = cvt_pk_bf16(v0[2], v0[3]); xw.z = cvt_pk_bf16(v1[0], v1[1]); xw.w = cvt_pk_bf16(v1[2], v1[3]); *(u32x4*)(C + off + bj * HALF) = xw; }
;                     const f32x4 h0 = v0 * gv[bj][0], h1 = v1 * gv[bj][1];
;                     u32x2 w; w.x = cvt_pk4_fp8(h0[0], h0[1], h0[2], h0[3]); w.y = cvt_pk4_fp8(h1[0], h1[1], h1[2], h1[3]);
;                     *(u32x2*)(H2 + off + bj * HALF) = w; } }
.LBB0_921:
	s_lshl_b32 s36, s52, 8
	v_mbcnt_lo_u32_b32 v96, -1, 0
	v_mbcnt_hi_u32_b32 v96, -1, v96
	s_add_i32 s36, s36, s34
	s_lshl_b32 s35, s35, 8
	v_ashrrev_i32_e32 v97, 1, v96
	s_or_b32 s35, s35, s84
	v_and_b32_e32 v97, -8, v97
	v_and_or_b32 v144, v96, 15, s36
	v_add_u32_e32 v148, s35, v97
	v_ashrrev_i32_e32 v145, 31, v144
	v_ashrrev_i32_e32 v149, 31, v148
	v_lshlrev_b64 v[96:97], 11, v[144:145]
	v_lshl_add_u64 v[146:147], v[96:97], 0, v[148:149]
	v_lshl_add_u64 v[168:169], v[146:147], 2, s[6:7]
	global_load_dwordx4 v[160:163], v[168:169], off
	global_load_dwordx4 v[164:167], v[168:169], off offset:16
	v_lshl_add_u64 v[100:101], v[148:149], 2, s[12:13]
	global_load_dwordx4 v[116:119], v[100:101], off
	global_load_dwordx4 v[112:115], v[100:101], off offset:16
	global_load_dwordx4 v[96:99], v[100:101], off offset:528
	s_nop 0
	global_load_dwordx4 v[100:103], v[100:101], off offset:512
	v_lshlrev_b32_e32 v232, 2, v146
	global_load_dwordx4 v[176:179], v232, s[6:7] offset:512
	global_load_dwordx4 v[180:183], v232, s[6:7] offset:528
	v_add_u32_e32 v233, 0x20000, v232
	global_load_dwordx4 v[184:187], v233, s[6:7]
	global_load_dwordx4 v[188:191], v233, s[6:7] offset:16
	v_add_u32_e32 v233, 0x20000, v232
	global_load_dwordx4 v[192:195], v233, s[6:7] offset:512
	global_load_dwordx4 v[196:199], v233, s[6:7] offset:528
	v_add_u32_e32 v233, 0x40000, v232
	global_load_dwordx4 v[200:203], v233, s[6:7]
	global_load_dwordx4 v[204:207], v233, s[6:7] offset:16
	v_add_u32_e32 v233, 0x40000, v232
	global_load_dwordx4 v[208:211], v233, s[6:7] offset:512
	global_load_dwordx4 v[212:215], v233, s[6:7] offset:528
	v_add_u32_e32 v233, 0x60000, v232
	global_load_dwordx4 v[216:219], v233, s[6:7]
	global_load_dwordx4 v[220:223], v233, s[6:7] offset:16
	v_add_u32_e32 v233, 0x60000, v232
	global_load_dwordx4 v[224:227], v233, s[6:7] offset:512
	global_load_dwordx4 v[228:231], v233, s[6:7] offset:528
	v_mov_b32_e32 v170, v145
	v_mov_b32_e32 v171, v145
	v_lshl_add_u64 v[172:173], v[146:147], 1, s[14:15]
	v_lshl_add_u64 v[174:175], s[10:11], 0, v[146:147]
	s_andn2_b64 vcc, exec, s[50:51]
	s_mov_b64 s[50:51], -1
	s_waitcnt vmcnt(19)
	v_pk_add_f32 v[140:141], v[140:141], v[160:161]
	s_waitcnt vmcnt(18)
	v_pk_add_f32 v[160:161], v[138:139], v[166:167]
	v_pk_add_f32 v[138:139], v[136:137], v[164:165]
	v_pk_add_f32 v[142:143], v[142:143], v[162:163]
	v_cvt_pk_bf16_f32 v136, v140, v141
	s_waitcnt vmcnt(17)
	v_pk_mul_f32 v[140:141], v[116:117], v[140:141]
	s_waitcnt vmcnt(16)
	v_pk_mul_f32 v[162:163], v[112:113], v[138:139]
	v_cvt_pk_fp8_f32 v170, v140, v141
	v_cvt_pk_fp8_f32 v171, v162, v163
	v_cvt_pk_bf16_f32 v137, v142, v143
	v_pk_mul_f32 v[140:141], v[118:119], v[142:143]
	v_pk_mul_f32 v[142:143], v[114:115], v[160:161]
	v_cvt_pk_fp8_f32 v170, v140, v141 op_sel:[0,0,1]
	v_cvt_pk_fp8_f32 v171, v142, v143 op_sel:[0,0,1]
	v_cvt_pk_bf16_f32 v138, v138, v139
	v_cvt_pk_bf16_f32 v139, v160, v161
	global_store_dwordx4 v[172:173], v[136:139], off
	global_store_dwordx2 v[174:175], v[170:171], off
	v_mov_b32_e32 v160, v145
	v_mov_b32_e32 v161, v145
	v_or_b32_e32 v162, 16, v144
	v_ashrrev_i32_e32 v163, 31, v162
	v_lshlrev_b64 v[162:163], 11, v[162:163]
	v_lshl_add_u64 v[162:163], v[162:163], 0, v[148:149]
	v_lshl_add_u64 v[164:165], v[162:163], 2, s[6:7]
	s_waitcnt vmcnt(14)
	v_pk_add_f32 v[132:133], v[132:133], v[176:177]
	v_pk_add_f32 v[136:137], v[130:131], v[182:183]
	v_pk_add_f32 v[130:131], v[128:129], v[180:181]
	v_pk_add_f32 v[134:135], v[134:135], v[178:179]
	v_add_u32_e32 v233, 0x100000, v232
	global_load_dwordx4 v[176:179], v233, s[6:7]
	global_load_dwordx4 v[180:183], v233, s[6:7] offset:16
	v_cvt_pk_bf16_f32 v128, v132, v133
	v_pk_mul_f32 v[132:133], v[100:101], v[132:133]
	v_pk_mul_f32 v[138:139], v[96:97], v[130:131]
	v_cvt_pk_fp8_f32 v160, v132, v133
	v_cvt_pk_fp8_f32 v161, v138, v139
	v_cvt_pk_bf16_f32 v129, v134, v135
	v_pk_mul_f32 v[132:133], v[102:103], v[134:135]
	v_pk_mul_f32 v[134:135], v[98:99], v[136:137]
	v_cvt_pk_fp8_f32 v160, v132, v133 op_sel:[0,0,1]
	v_cvt_pk_fp8_f32 v161, v134, v135 op_sel:[0,0,1]
	v_cvt_pk_bf16_f32 v130, v130, v131
	v_cvt_pk_bf16_f32 v131, v136, v137
	global_store_dwordx4 v[172:173], v[128:131], off offset:256
	global_store_dwordx2 v[174:175], v[160:161], off offset:128
	v_mov_b32_e32 v136, v145
	v_mov_b32_e32 v137, v145
	v_lshl_add_u64 v[138:139], v[162:163], 1, s[14:15]
	v_lshl_add_u64 v[140:141], s[10:11], 0, v[162:163]
	s_waitcnt vmcnt(16)
	v_pk_add_f32 v[124:125], v[124:125], v[184:185]
	v_pk_add_f32 v[128:129], v[122:123], v[190:191]
	v_pk_add_f32 v[122:123], v[120:121], v[188:189]
	v_pk_add_f32 v[126:127], v[126:127], v[186:187]
	v_add_u32_e32 v233, 0x100000, v232
	global_load_dwordx4 v[184:187], v233, s[6:7] offset:512
	global_load_dwordx4 v[188:191], v233, s[6:7] offset:528
	v_cvt_pk_bf16_f32 v120, v124, v125
	v_pk_mul_f32 v[124:125], v[116:117], v[124:125]
	v_pk_mul_f32 v[130:131], v[112:113], v[122:123]
	v_cvt_pk_fp8_f32 v136, v124, v125
	v_cvt_pk_fp8_f32 v137, v130, v131
	v_cvt_pk_bf16_f32 v121, v126, v127
	v_pk_mul_f32 v[124:125], v[118:119], v[126:127]
	v_pk_mul_f32 v[126:127], v[114:115], v[128:129]
	v_cvt_pk_fp8_f32 v136, v124, v125 op_sel:[0,0,1]
	v_cvt_pk_fp8_f32 v137, v126, v127 op_sel:[0,0,1]
	v_cvt_pk_bf16_f32 v122, v122, v123
	v_cvt_pk_bf16_f32 v123, v128, v129
	global_store_dwordx4 v[138:139], v[120:123], off
	global_store_dwordx2 v[140:141], v[136:137], off
	v_mov_b32_e32 v128, v145
	v_mov_b32_e32 v129, v145
	v_or_b32_e32 v130, 32, v144
	v_ashrrev_i32_e32 v131, 31, v130
	v_lshlrev_b64 v[130:131], 11, v[130:131]
	v_lshl_add_u64 v[130:131], v[130:131], 0, v[148:149]
	v_lshl_add_u64 v[132:133], v[130:131], 2, s[6:7]
	s_waitcnt vmcnt(18)
; __device__ __forceinline__ unsigned cvt_pk_bf16(float lo, float hi) { unsigned r; asm volatile("v_cvt_pk_bf16_f32 %0, %1, %2" : "=v"(r) : "v"(lo), "v"(hi)); return r; }
; __device__ __forceinline__ unsigned cvt_pk4_fp8(float a, float b, float c, float d) { int w; asm("" : "=v"(w));     w = __builtin_amdgcn_cvt_pk_fp8_f32(a, b, w, false); w = __builtin_amdgcn_cvt_pk_fp8_f32(c, d, w, true); return (unsigned)w; }
;     __device__ __forceinline__ void operator()(const f32x4 (&acc)[2][2][4][2], const Unit& u, int wr, int wc, int fr, int fq) const {
;     ...
;         for (int ai = 0; ai < 2; ++ai)
; #pragma unroll
;             for (int m = 0; m < 4; ++m) { const size_t off = (size_t)(row0 + ai * HALF + m * 16) * DM + col0;
; #pragma unroll
;                 for (int bj = 0; bj < 2; ++bj) { const f32x4 v0 = *(const f32x4*)(base + off + bj * HALF) + acc[ai][bj][m][0], v1 = *(const f32x4*)(base + off + bj * HALF + 4) + acc[ai][bj][m][1];
;                     { u32x4 xw; xw.x = cvt_pk_bf16(v0[0], v0[1]); xw.y = cvt_pk_bf16(v0[2], v0[3]); xw.z = cvt_pk_bf16(v1[0], v1[1]); xw.w = cvt_pk_bf16(v1[2], v1[3]); *(u32x4*)(C + off + bj * HALF) = xw; }
;                     const f32x4 h0 = v0 * gv[bj][0], h1 = v1 * gv[bj][1];
;                     u32x2 w; w.x = cvt_pk4_fp8(h0[0], h0[1], h0[2], h0[3]); w.y = cvt_pk4_fp8(h1[0], h1[1], h1[2], h1[3]);
;                     *(u32x2*)(H2 + off + bj * HALF) = w; } }
	v_pk_add_f32 v[108:109], v[108:109], v[192:193]
	v_pk_add_f32 v[120:121], v[106:107], v[198:199]
	v_pk_add_f32 v[106:107], v[104:105], v[196:197]
	v_pk_add_f32 v[110:111], v[110:111], v[194:195]
	v_add_u32_e32 v233, 0x120000, v232
	global_load_dwordx4 v[192:195], v233, s[6:7]
	global_load_dwordx4 v[196:199], v233, s[6:7] offset:16
	v_cvt_pk_bf16_f32 v104, v108, v109
	v_pk_mul_f32 v[108:109], v[100:101], v[108:109]
	v_pk_mul_f32 v[122:123], v[96:97], v[106:107]
	v_cvt_pk_fp8_f32 v128, v108, v109
	v_cvt_pk_fp8_f32 v129, v122, v123
	v_cvt_pk_bf16_f32 v105, v110, v111
	v_pk_mul_f32 v[108:109], v[102:103], v[110:111]
	v_pk_mul_f32 v[110:111], v[98:99], v[120:121]
	v_cvt_pk_fp8_f32 v128, v108, v109 op_sel:[0,0,1]
	v_cvt_pk_fp8_f32 v129, v110, v111 op_sel:[0,0,1]
	v_cvt_pk_bf16_f32 v106, v106, v107
	v_cvt_pk_bf16_f32 v107, v120, v121
	global_store_dwordx4 v[138:139], v[104:107], off offset:256
	global_store_dwordx2 v[140:141], v[128:129], off offset:128
	v_mov_b32_e32 v120, v145
	v_mov_b32_e32 v121, v145
	v_lshl_add_u64 v[122:123], v[130:131], 1, s[14:15]
	v_lshl_add_u64 v[124:125], s[10:11], 0, v[130:131]
	s_waitcnt vmcnt(20)
	v_pk_add_f32 v[92:93], v[92:93], v[200:201]
	v_pk_add_f32 v[104:105], v[90:91], v[206:207]
	v_pk_add_f32 v[90:91], v[88:89], v[204:205]
	v_pk_add_f32 v[94:95], v[94:95], v[202:203]
	v_add_u32_e32 v233, 0x120000, v232
	global_load_dwordx4 v[200:203], v233, s[6:7] offset:512
	global_load_dwordx4 v[204:207], v233, s[6:7] offset:528
	v_cvt_pk_bf16_f32 v88, v92, v93
	v_pk_mul_f32 v[92:93], v[116:117], v[92:93]
	v_pk_mul_f32 v[106:107], v[112:113], v[90:91]
	v_cvt_pk_fp8_f32 v120, v92, v93
	v_cvt_pk_fp8_f32 v121, v106, v107
	v_cvt_pk_bf16_f32 v89, v94, v95
	v_pk_mul_f32 v[92:93], v[118:119], v[94:95]
	v_pk_mul_f32 v[94:95], v[114:115], v[104:105]
	v_cvt_pk_fp8_f32 v120, v92, v93 op_sel:[0,0,1]
	v_cvt_pk_fp8_f32 v121, v94, v95 op_sel:[0,0,1]
	v_cvt_pk_bf16_f32 v90, v90, v91
	v_cvt_pk_bf16_f32 v91, v104, v105
	global_store_dwordx4 v[122:123], v[88:91], off
	global_store_dwordx2 v[124:125], v[120:121], off
	v_mov_b32_e32 v104, v145
	v_mov_b32_e32 v105, v145
	v_or_b32_e32 v106, 48, v144
	v_ashrrev_i32_e32 v107, 31, v106
	v_lshlrev_b64 v[106:107], 11, v[106:107]
	v_lshl_add_u64 v[106:107], v[106:107], 0, v[148:149]
	v_lshl_add_u64 v[108:109], v[106:107], 2, s[6:7]
	v_mov_b32_e32 v144, v145
	s_waitcnt vmcnt(22)
	v_pk_add_f32 v[84:85], v[84:85], v[208:209]
	v_pk_add_f32 v[88:89], v[82:83], v[214:215]
	v_pk_add_f32 v[82:83], v[80:81], v[212:213]
	v_pk_add_f32 v[86:87], v[86:87], v[210:211]
	v_add_u32_e32 v233, 0x140000, v232
	global_load_dwordx4 v[208:211], v233, s[6:7]
	global_load_dwordx4 v[212:215], v233, s[6:7] offset:16
	v_cvt_pk_bf16_f32 v80, v84, v85
	v_pk_mul_f32 v[84:85], v[100:101], v[84:85]
	v_pk_mul_f32 v[90:91], v[96:97], v[82:83]
	v_cvt_pk_fp8_f32 v104, v84, v85
	v_cvt_pk_fp8_f32 v105, v90, v91
	v_cvt_pk_bf16_f32 v81, v86, v87
	v_pk_mul_f32 v[84:85], v[102:103], v[86:87]
	v_pk_mul_f32 v[86:87], v[98:99], v[88:89]
	v_cvt_pk_fp8_f32 v104, v84, v85 op_sel:[0,0,1]
	v_cvt_pk_fp8_f32 v105, v86, v87 op_sel:[0,0,1]
	v_cvt_pk_bf16_f32 v82, v82, v83
	v_cvt_pk_bf16_f32 v83, v88, v89
	global_store_dwordx4 v[122:123], v[80:83], off offset:256
	global_store_dwordx2 v[124:125], v[104:105], off offset:128
	v_mov_b32_e32 v88, v145
	v_mov_b32_e32 v89, v145
	v_lshl_add_u64 v[90:91], v[106:107], 1, s[14:15]
	v_lshl_add_u64 v[92:93], s[10:11], 0, v[106:107]
	s_waitcnt vmcnt(24)
	v_pk_add_f32 v[76:77], v[76:77], v[216:217]
	v_pk_add_f32 v[80:81], v[74:75], v[222:223]
	v_pk_add_f32 v[74:75], v[72:73], v[220:221]
	v_pk_add_f32 v[78:79], v[78:79], v[218:219]
	v_add_u32_e32 v233, 0x140000, v232
	global_load_dwordx4 v[216:219], v233, s[6:7] offset:512
	global_load_dwordx4 v[220:223], v233, s[6:7] offset:528
	v_cvt_pk_bf16_f32 v72, v76, v77
	v_pk_mul_f32 v[76:77], v[116:117], v[76:77]
	v_pk_mul_f32 v[82:83], v[112:113], v[74:75]
	v_cvt_pk_fp8_f32 v88, v76, v77
	v_cvt_pk_fp8_f32 v89, v82, v83
	v_cvt_pk_bf16_f32 v73, v78, v79
	v_pk_mul_f32 v[76:77], v[118:119], v[78:79]
	v_pk_mul_f32 v[78:79], v[114:115], v[80:81]
	v_cvt_pk_fp8_f32 v88, v76, v77 op_sel:[0,0,1]
	v_cvt_pk_fp8_f32 v89, v78, v79 op_sel:[0,0,1]
	v_cvt_pk_bf16_f32 v74, v74, v75
	v_cvt_pk_bf16_f32 v75, v80, v81
	global_store_dwordx4 v[90:91], v[72:75], off
	global_store_dwordx2 v[92:93], v[88:89], off
	v_mov_b32_e32 v80, v145
	v_mov_b32_e32 v81, v145
	v_lshl_add_u64 v[82:83], v[146:147], 0, s[20:21]
	v_lshl_add_u64 v[84:85], v[82:83], 2, s[6:7]
	s_waitcnt vmcnt(26)
	v_pk_add_f32 v[68:69], v[68:69], v[224:225]
	v_pk_add_f32 v[72:73], v[66:67], v[230:231]
	v_pk_add_f32 v[66:67], v[64:65], v[228:229]
	v_pk_add_f32 v[70:71], v[70:71], v[226:227]
	v_add_u32_e32 v233, 0x160000, v232
	global_load_dwordx4 v[224:227], v233, s[6:7]
	global_load_dwordx4 v[228:231], v233, s[6:7] offset:16
	v_cvt_pk_bf16_f32 v64, v68, v69
	v_pk_mul_f32 v[68:69], v[100:101], v[68:69]
	v_pk_mul_f32 v[74:75], v[96:97], v[66:67]
	v_cvt_pk_fp8_f32 v80, v68, v69
	v_cvt_pk_fp8_f32 v81, v74, v75
	v_cvt_pk_bf16_f32 v65, v70, v71
	v_pk_mul_f32 v[68:69], v[102:103], v[70:71]
	v_pk_mul_f32 v[70:71], v[98:99], v[72:73]
	v_cvt_pk_fp8_f32 v80, v68, v69 op_sel:[0,0,1]
	v_cvt_pk_fp8_f32 v81, v70, v71 op_sel:[0,0,1]
	v_cvt_pk_bf16_f32 v66, v66, v67
	v_cvt_pk_bf16_f32 v67, v72, v73
	global_store_dwordx4 v[90:91], v[64:67], off offset:256
	global_store_dwordx2 v[92:93], v[80:81], off offset:128
	v_mov_b32_e32 v72, v145
	v_mov_b32_e32 v73, v145
	v_lshl_add_u64 v[74:75], v[82:83], 1, s[14:15]
	v_lshl_add_u64 v[76:77], s[10:11], 0, v[82:83]
	s_waitcnt vmcnt(26)
; __device__ __forceinline__ unsigned cvt_pk_bf16(float lo, float hi) { unsigned r; asm volatile("v_cvt_pk_bf16_f32 %0, %1, %2" : "=v"(r) : "v"(lo), "v"(hi)); return r; }
; __device__ __forceinline__ unsigned cvt_pk4_fp8(float a, float b, float c, float d) { int w; asm("" : "=v"(w));     w = __builtin_amdgcn_cvt_pk_fp8_f32(a, b, w, false); w = __builtin_amdgcn_cvt_pk_fp8_f32(c, d, w, true); return (unsigned)w; }
;     __device__ __forceinline__ void operator()(const f32x4 (&acc)[2][2][4][2], const Unit& u, int wr, int wc, int fr, int fq) const {
;     ...
;         for (int ai = 0; ai < 2; ++ai)
; #pragma unroll
;             for (int m = 0; m < 4; ++m) { const size_t off = (size_t)(row0 + ai * HALF + m * 16) * DM + col0;
; #pragma unroll
;                 for (int bj = 0; bj < 2; ++bj) { const f32x4 v0 = *(const f32x4*)(base + off + bj * HALF) + acc[ai][bj][m][0], v1 = *(const f32x4*)(base + off + bj * HALF + 4) + acc[ai][bj][m][1];
;                     { u32x4 xw; xw.x = cvt_pk_bf16(v0[0], v0[1]); xw.y = cvt_pk_bf16(v0[2], v0[3]); xw.z = cvt_pk_bf16(v1[0], v1[1]); xw.w = cvt_pk_bf16(v1[2], v1[3]); *(u32x4*)(C + off + bj * HALF) = xw; }
;                     const f32x4 h0 = v0 * gv[bj][0], h1 = v1 * gv[bj][1];
;                     u32x2 w; w.x = cvt_pk4_fp8(h0[0], h0[1], h0[2], h0[3]); w.y = cvt_pk4_fp8(h1[0], h1[1], h1[2], h1[3]);
;                     *(u32x2*)(H2 + off + bj * HALF) = w; } }
	v_pk_add_f32 v[60:61], v[60:61], v[176:177]
	v_pk_add_f32 v[64:65], v[58:59], v[182:183]
	v_pk_add_f32 v[58:59], v[56:57], v[180:181]
	v_pk_add_f32 v[62:63], v[62:63], v[178:179]
	v_add_u32_e32 v233, 0x160000, v232
	global_load_dwordx4 v[176:179], v233, s[6:7] offset:512
	global_load_dwordx4 v[180:183], v233, s[6:7] offset:528
	v_cvt_pk_bf16_f32 v56, v60, v61
	v_pk_mul_f32 v[60:61], v[116:117], v[60:61]
	v_pk_mul_f32 v[66:67], v[112:113], v[58:59]
	v_cvt_pk_fp8_f32 v72, v60, v61
	v_cvt_pk_fp8_f32 v73, v66, v67
	v_cvt_pk_bf16_f32 v57, v62, v63
	v_pk_mul_f32 v[60:61], v[118:119], v[62:63]
	v_pk_mul_f32 v[62:63], v[114:115], v[64:65]
	v_cvt_pk_fp8_f32 v72, v60, v61 op_sel:[0,0,1]
	v_cvt_pk_fp8_f32 v73, v62, v63 op_sel:[0,0,1]
	v_cvt_pk_bf16_f32 v58, v58, v59
	v_cvt_pk_bf16_f32 v59, v64, v65
	global_store_dwordx4 v[74:75], v[56:59], off
	global_store_dwordx2 v[76:77], v[72:73], off
	v_mov_b32_e32 v64, v145
	v_mov_b32_e32 v65, v145
	v_lshl_add_u64 v[66:67], v[146:147], 0, s[22:23]
	v_lshl_add_u64 v[68:69], v[66:67], 2, s[6:7]
	s_waitcnt vmcnt(26)
	v_pk_add_f32 v[52:53], v[52:53], v[184:185]
	v_pk_add_f32 v[56:57], v[50:51], v[190:191]
	v_pk_add_f32 v[50:51], v[48:49], v[188:189]
	v_pk_add_f32 v[54:55], v[54:55], v[186:187]
	v_cvt_pk_bf16_f32 v48, v52, v53
	v_pk_mul_f32 v[52:53], v[100:101], v[52:53]
	v_pk_mul_f32 v[58:59], v[96:97], v[50:51]
	v_cvt_pk_fp8_f32 v64, v52, v53
	v_cvt_pk_fp8_f32 v65, v58, v59
	v_cvt_pk_bf16_f32 v49, v54, v55
	v_pk_mul_f32 v[52:53], v[102:103], v[54:55]
	v_pk_mul_f32 v[54:55], v[98:99], v[56:57]
	v_cvt_pk_fp8_f32 v64, v52, v53 op_sel:[0,0,1]
	v_cvt_pk_fp8_f32 v65, v54, v55 op_sel:[0,0,1]
	v_cvt_pk_bf16_f32 v50, v50, v51
	v_cvt_pk_bf16_f32 v51, v56, v57
	global_store_dwordx4 v[74:75], v[48:51], off offset:256
	global_store_dwordx2 v[76:77], v[64:65], off offset:128
	v_mov_b32_e32 v56, v145
	v_mov_b32_e32 v57, v145
	v_lshl_add_u64 v[58:59], v[66:67], 1, s[14:15]
	v_lshl_add_u64 v[60:61], s[10:11], 0, v[66:67]
	s_waitcnt vmcnt(24)
	v_pk_add_f32 v[44:45], v[44:45], v[192:193]
	v_pk_add_f32 v[48:49], v[42:43], v[198:199]
	v_pk_add_f32 v[42:43], v[40:41], v[196:197]
	v_pk_add_f32 v[46:47], v[46:47], v[194:195]
	v_cvt_pk_bf16_f32 v40, v44, v45
	v_pk_mul_f32 v[44:45], v[116:117], v[44:45]
	v_pk_mul_f32 v[50:51], v[112:113], v[42:43]
	v_cvt_pk_fp8_f32 v56, v44, v45
	v_cvt_pk_fp8_f32 v57, v50, v51
	v_cvt_pk_bf16_f32 v41, v46, v47
	v_pk_mul_f32 v[44:45], v[118:119], v[46:47]
	v_pk_mul_f32 v[46:47], v[114:115], v[48:49]
	v_cvt_pk_fp8_f32 v56, v44, v45 op_sel:[0,0,1]
	v_cvt_pk_fp8_f32 v57, v46, v47 op_sel:[0,0,1]
	v_cvt_pk_bf16_f32 v42, v42, v43
	v_cvt_pk_bf16_f32 v43, v48, v49
	global_store_dwordx4 v[58:59], v[40:43], off
	global_store_dwordx2 v[60:61], v[56:57], off
	v_mov_b32_e32 v48, v145
	v_mov_b32_e32 v49, v145
	v_lshl_add_u64 v[50:51], v[146:147], 0, s[24:25]
	v_lshl_add_u64 v[52:53], v[50:51], 2, s[6:7]
	s_waitcnt vmcnt(22)
	v_pk_add_f32 v[36:37], v[36:37], v[200:201]
	v_pk_add_f32 v[40:41], v[34:35], v[206:207]
	v_pk_add_f32 v[34:35], v[32:33], v[204:205]
	v_pk_add_f32 v[38:39], v[38:39], v[202:203]
	v_cvt_pk_bf16_f32 v32, v36, v37
	v_pk_mul_f32 v[36:37], v[100:101], v[36:37]
	v_pk_mul_f32 v[42:43], v[96:97], v[34:35]
	v_cvt_pk_fp8_f32 v48, v36, v37
	v_cvt_pk_fp8_f32 v49, v42, v43
	v_cvt_pk_bf16_f32 v33, v38, v39
	v_pk_mul_f32 v[36:37], v[102:103], v[38:39]
	v_pk_mul_f32 v[38:39], v[98:99], v[40:41]
	v_cvt_pk_fp8_f32 v48, v36, v37 op_sel:[0,0,1]
	v_cvt_pk_fp8_f32 v49, v38, v39 op_sel:[0,0,1]
	v_cvt_pk_bf16_f32 v34, v34, v35
	v_cvt_pk_bf16_f32 v35, v40, v41
	global_store_dwordx4 v[58:59], v[32:35], off offset:256
	global_store_dwordx2 v[60:61], v[48:49], off offset:128
	v_mov_b32_e32 v40, v145
	v_mov_b32_e32 v41, v145
	v_lshl_add_u64 v[42:43], v[50:51], 1, s[14:15]
	v_lshl_add_u64 v[44:45], s[10:11], 0, v[50:51]
	s_waitcnt vmcnt(20)
; __device__ __forceinline__ unsigned cvt_pk_bf16(float lo, float hi) { unsigned r; asm volatile("v_cvt_pk_bf16_f32 %0, %1, %2" : "=v"(r) : "v"(lo), "v"(hi)); return r; }
; __device__ __forceinline__ unsigned cvt_pk4_fp8(float a, float b, float c, float d) { int w; asm("" : "=v"(w));     w = __builtin_amdgcn_cvt_pk_fp8_f32(a, b, w, false); w = __builtin_amdgcn_cvt_pk_fp8_f32(c, d, w, true); return (unsigned)w; }
; #define PG8_BAR __builtin_amdgcn_s_barrier()
;     __device__ __forceinline__ void operator()(const f32x4 (&acc)[2][2][4][2], const Unit& u, int wr, int wc, int fr, int fq) const {
;     ...
;         for (int ai = 0; ai < 2; ++ai)
; #pragma unroll
;             for (int m = 0; m < 4; ++m) { const size_t off = (size_t)(row0 + ai * HALF + m * 16) * DM + col0;
; #pragma unroll
;                 for (int bj = 0; bj < 2; ++bj) { const f32x4 v0 = *(const f32x4*)(base + off + bj * HALF) + acc[ai][bj][m][0], v1 = *(const f32x4*)(base + off + bj * HALF + 4) + acc[ai][bj][m][1];
;                     { u32x4 xw; xw.x = cvt_pk_bf16(v0[0], v0[1]); xw.y = cvt_pk_bf16(v0[2], v0[3]); xw.z = cvt_pk_bf16(v1[0], v1[1]); xw.w = cvt_pk_bf16(v1[2], v1[3]); *(u32x4*)(C + off + bj * HALF) = xw; }
;                     const f32x4 h0 = v0 * gv[bj][0], h1 = v1 * gv[bj][1];
;                     u32x2 w; w.x = cvt_pk4_fp8(h0[0], h0[1], h0[2], h0[3]); w.y = cvt_pk4_fp8(h1[0], h1[1], h1[2], h1[3]);
;                     *(u32x2*)(H2 + off + bj * HALF) = w; } }
; template <bool FP8 = false, class Epi, class Sched>
; __device__ __forceinline__ void gemm_phase(LAS unsigned char* lds, const int K, const int lda, const int ldb, const Sched& S, const Epi& E, const int wid) {
;     ...
;         if (!has_next) break;
; #pragma unroll
;         for (int a = 0; a < 2; ++a)
; #pragma unroll
;             for (int b = 0; b < 2; ++b)
; #pragma unroll
;                 for (int m = 0; m < 4; ++m)
; #pragma unroll
;                     for (int n = 0; n < 2; ++n) acc[a][b][m][n] = (f32x4){0.f, 0.f, 0.f, 0.f};
;         cur = nxt; cA = nA; cB = nB; ++ui;
;         if (wr == 1) PG8_BAR;
	v_pk_add_f32 v[28:29], v[28:29], v[208:209]
	v_pk_add_f32 v[32:33], v[26:27], v[214:215]
	v_pk_add_f32 v[26:27], v[24:25], v[212:213]
	v_pk_add_f32 v[30:31], v[30:31], v[210:211]
	v_cvt_pk_bf16_f32 v24, v28, v29
	v_pk_mul_f32 v[28:29], v[116:117], v[28:29]
	v_pk_mul_f32 v[34:35], v[112:113], v[26:27]
	v_cvt_pk_fp8_f32 v40, v28, v29
	v_cvt_pk_fp8_f32 v41, v34, v35
	v_cvt_pk_bf16_f32 v25, v30, v31
	v_pk_mul_f32 v[28:29], v[118:119], v[30:31]
	v_pk_mul_f32 v[30:31], v[114:115], v[32:33]
	v_cvt_pk_fp8_f32 v40, v28, v29 op_sel:[0,0,1]
	v_cvt_pk_fp8_f32 v41, v30, v31 op_sel:[0,0,1]
	v_cvt_pk_bf16_f32 v26, v26, v27
	v_cvt_pk_bf16_f32 v27, v32, v33
	global_store_dwordx4 v[42:43], v[24:27], off
	global_store_dwordx2 v[44:45], v[40:41], off
	v_mov_b32_e32 v32, v145
	v_mov_b32_e32 v33, v145
	v_lshl_add_u64 v[34:35], v[146:147], 0, s[26:27]
	v_lshl_add_u64 v[36:37], v[34:35], 2, s[6:7]
	s_waitcnt vmcnt(18)
	v_pk_add_f32 v[20:21], v[20:21], v[216:217]
	v_pk_add_f32 v[24:25], v[18:19], v[222:223]
	v_pk_add_f32 v[18:19], v[16:17], v[220:221]
	v_pk_add_f32 v[22:23], v[22:23], v[218:219]
	v_cvt_pk_bf16_f32 v16, v20, v21
	v_pk_mul_f32 v[20:21], v[100:101], v[20:21]
	v_pk_mul_f32 v[26:27], v[96:97], v[18:19]
	v_cvt_pk_fp8_f32 v32, v20, v21
	v_cvt_pk_fp8_f32 v33, v26, v27
	v_cvt_pk_bf16_f32 v17, v22, v23
	v_pk_mul_f32 v[20:21], v[102:103], v[22:23]
	v_pk_mul_f32 v[22:23], v[98:99], v[24:25]
	v_cvt_pk_fp8_f32 v32, v20, v21 op_sel:[0,0,1]
	v_cvt_pk_fp8_f32 v33, v22, v23 op_sel:[0,0,1]
	v_cvt_pk_bf16_f32 v18, v18, v19
	v_cvt_pk_bf16_f32 v19, v24, v25
	global_store_dwordx4 v[42:43], v[16:19], off offset:256
	global_store_dwordx2 v[44:45], v[32:33], off offset:128
	v_mov_b32_e32 v24, v145
	v_mov_b32_e32 v25, v145
	v_lshl_add_u64 v[26:27], v[34:35], 1, s[14:15]
	v_lshl_add_u64 v[28:29], s[10:11], 0, v[34:35]
	s_waitcnt vmcnt(16)
	v_pk_add_f32 v[12:13], v[12:13], v[224:225]
	v_pk_add_f32 v[16:17], v[10:11], v[230:231]
	v_pk_add_f32 v[10:11], v[8:9], v[228:229]
	v_pk_add_f32 v[14:15], v[14:15], v[226:227]
	v_cvt_pk_bf16_f32 v8, v12, v13
	v_pk_mul_f32 v[12:13], v[116:117], v[12:13]
	v_pk_mul_f32 v[18:19], v[112:113], v[10:11]
	v_cvt_pk_fp8_f32 v24, v12, v13
	v_cvt_pk_fp8_f32 v25, v18, v19
	v_cvt_pk_bf16_f32 v9, v14, v15
	v_pk_mul_f32 v[12:13], v[118:119], v[14:15]
	v_pk_mul_f32 v[14:15], v[114:115], v[16:17]
	v_cvt_pk_fp8_f32 v24, v12, v13 op_sel:[0,0,1]
	v_cvt_pk_fp8_f32 v25, v14, v15 op_sel:[0,0,1]
	v_cvt_pk_bf16_f32 v10, v10, v11
	v_cvt_pk_bf16_f32 v11, v16, v17
	global_store_dwordx4 v[26:27], v[8:11], off
	global_store_dwordx2 v[28:29], v[24:25], off
	s_waitcnt vmcnt(14)
	v_pk_add_f32 v[4:5], v[4:5], v[176:177]
	v_pk_add_f32 v[8:9], v[2:3], v[182:183]
	v_pk_add_f32 v[2:3], v[0:1], v[180:181]
	v_pk_add_f32 v[6:7], v[6:7], v[178:179]
	v_cvt_pk_bf16_f32 v0, v4, v5
	v_pk_mul_f32 v[4:5], v[100:101], v[4:5]
	v_pk_mul_f32 v[10:11], v[96:97], v[2:3]
	v_cvt_pk_fp8_f32 v144, v4, v5
	v_cvt_pk_fp8_f32 v145, v10, v11
	v_cvt_pk_bf16_f32 v1, v6, v7
	v_pk_mul_f32 v[4:5], v[102:103], v[6:7]
	v_pk_mul_f32 v[6:7], v[98:99], v[8:9]
	v_cvt_pk_fp8_f32 v144, v4, v5 op_sel:[0,0,1]
	v_cvt_pk_fp8_f32 v145, v6, v7 op_sel:[0,0,1]
	v_cvt_pk_bf16_f32 v2, v2, v3
	v_cvt_pk_bf16_f32 v3, v8, v9
	global_store_dwordx4 v[26:27], v[0:3], off offset:256
	global_store_dwordx2 v[28:29], v[144:145], off offset:128
	s_cbranch_vccnz .LBB0_910
	s_andn2_b64 vcc, exec, s[16:17]
	s_cbranch_vccnz .LBB0_909
	s_barrier
	s_branch .LBB0_909

; #define LAS __attribute__((address_space(3)))
; #define LANE_TID() const int lane = lane_id(), tid = wave * 64 + lane
; __global__ void __launch_bounds__(512, 2) fwd_kernel(Params p) {
;     ...
;     if (IN(8)) { LANE_TID();
;         LAS float* part = (LAS float*)lds;
;         LAS float* ssq = (LAS float*)(lds + 36864);
;         LAS int* lrk = (LAS int*)(lds + 40960);
;         LAS int* hist = (LAS int*)(lds + 53760);
;         LAS int* base = (LAS int*)(lds + 54016);
;         unsigned* cnt = ctl + CW_CNT;
;         for (int blk = vcu; blk < T / 64; blk += G) {
;             const int tt = wave & 1, kq = wave >> 1, j = lane & 31, hh = lane >> 5;
;             if (tid < 32) hist[tid] = 0;
;             {
;                 const bf16_t* xr = X1 + (size_t)(blk * 64 + tt * 32 + j) * DM + kq * 512 + hh * 4;
;                 const float* wr_ = WrT + (size_t)j * DM + kq * 512 + hh * 4;
;                 f32x16 acc = {}; float ss = 0.f;
.LBB0_979:
	s_or_b64 exec, exec, s[4:5]
	s_add_u32 s24, s28, 0xa7000000
	s_addc_u32 s25, s29, 0
	s_add_u32 s16, s28, 0x3000000
	s_addc_u32 s17, s29, 0
	s_add_u32 s18, s28, 0x3080000
	s_addc_u32 s19, s29, 0
	s_add_u32 s22, s28, 0xa6800000
	s_addc_u32 s23, s29, 0
	s_add_u32 s26, s28, 0xa6a00000
	s_addc_u32 s27, s29, 0
	v_readlane_b32 s0, v252, 17
	s_add_u32 s20, s28, 0x8000
	v_readlane_b32 s1, v252, 18
	s_addc_u32 s21, s29, 0
	s_andn2_b64 vcc, exec, s[0:1]
	s_waitcnt lgkmcnt(0)
	s_barrier
	s_nop 0
	v_mbcnt_lo_u32_b32 v0, -1, 0
	v_mbcnt_hi_u32_b32 v0, -1, v0
	s_cbranch_vccnz .LBB0_992
	s_add_u32 s42, s28, 0x3040000
	s_addc_u32 s43, s29, 0
	s_add_u32 s44, s28, 0x31a0000
	v_readlane_b32 s0, v252, 3
	s_addc_u32 s45, s29, 0
	s_lshr_b32 s3, s79, 7
	s_waitcnt vmcnt(10)
	v_add_u32_e32 v84, s0, v0
	v_ashrrev_i32_e32 v6, 5, v0
	s_and_b32 s8, s40, 32
	s_lshl_b32 s0, s3, 9
	s_lshl_b32 s6, s3, 10
	s_add_u32 s6, s14, s6
	v_lshlrev_b32_e32 v2, 2, v6
	s_addc_u32 s7, s15, 0
	v_ashrrev_i32_e32 v3, 31, v2
	v_and_b32_e32 v1, 31, v0
	s_waitcnt vmcnt(9)
	v_lshl_add_u64 v[88:89], v[2:3], 1, s[6:7]
	v_readlane_b32 s6, v252, 8
	v_mov_b32_e32 v87, 0
	v_lshlrev_b32_e32 v86, 13, v1
	v_readlane_b32 s7, v252, 9
	s_mov_b32 s1, 0
	v_or_b32_e32 v133, s8, v1
	v_lshl_add_u64 v[4:5], s[6:7], 0, v[86:87]
	v_lshl_add_u64 v[4:5], s[0:1], 2, v[4:5]
	s_lshl_b32 s0, s3, 6
	s_or_b32 s0, s8, s0
	v_or_b32_e32 v1, s0, v1
	s_movk_i32 s0, 0x84
	v_lshl_add_u64 v[90:91], v[2:3], 2, v[4:5]
	v_mul_lo_u32 v3, v1, s0
	v_lshlrev_b32_e32 v1, 3, v1
	v_add3_u32 v86, 0, v1, v2
	v_ashrrev_i32_e32 v1, 31, v0
	s_cmpk_lt_u32 s79, 0x4000
	v_lshlrev_b64 v[0:1], 4, v[0:1]
	v_readlane_b32 s1, v252, 2
	s_cselect_b64 s[40:41], -1, 0
	v_lshl_add_u64 v[94:95], s[10:11], 0, v[0:1]
	v_lshl_add_u64 v[96:97], s[24:25], 0, v[0:1]
	v_mul_lo_u32 v1, v84, s0
	s_lshl_b32 s0, s1, 2
	s_add_i32 s31, s0, 0
	s_add_i32 s0, s1, 56
	s_lshr_b32 s49, s0, 2
	s_add_i32 s0, s1, 48
	s_lshr_b32 s50, s0, 2
	s_add_i32 s0, s1, 40
	s_load_dwordx2 s[38:39], s[88:89], 0x88
	s_lshr_b32 s51, s0, 2
	s_add_i32 s0, s1, 32
	s_lshr_b32 s52, s0, 2
	s_add_i32 s0, s1, 24
	v_ashrrev_i32_e32 v85, 31, v84
	v_lshlrev_b32_e32 v0, 4, v6
	s_lshr_b32 s53, s0, 2
	s_add_i32 s0, s1, 16
	v_lshl_add_u64 v[92:93], v[84:85], 2, s[20:21]
	v_add3_u32 v85, 0, v3, v0
	v_lshlrev_b32_e32 v0, 3, v84
	s_lshr_b32 s54, s0, 2
	s_add_i32 s0, s1, 8
	v_cmp_gt_i32_e64 s[4:5], 32, v84
	v_lshl_add_u32 v132, v84, 2, 0
	v_cmp_gt_i32_e64 s[6:7], 64, v84
	v_lshlrev_b32_e32 v134, 4, v84
	v_add_u32_e32 v135, 0, v1
	s_add_i32 s31, s31, 0xa000
	s_lshl_b32 s37, s78, 6
	s_lshl_b32 s48, s33, 6
	s_lshr_b32 s55, s0, 2
	s_sub_i32 s56, s1, 64
	v_add_u32_e32 v136, 0, v0
	v_mov_b32_e32 v137, 0x358637bd
	s_mov_b32 s57, 0x800000
	s_mov_b32 s58, 0xff800000
	v_mov_b32_e32 v138, 1
	s_movk_i32 s59, 0x800
	s_movk_i32 s60, 0x1000
	s_movk_i32 s61, 0x2000
	s_mov_b32 s62, 0x8000
	s_mov_b32 s63, 0x10000
	s_mov_b32 s64, 0x20000
	s_mov_b32 s65, 0x40000
	s_mov_b32 s66, 0x80000
	s_mov_b32 s67, 0x100000
	s_mov_b32 s68, 0x200000
	s_mov_b32 s69, 0x400000
	s_mov_b32 s70, 0x1000000
	s_brev_b32 s71, 64
	s_brev_b32 s72, 32
	s_brev_b32 s73, 16
	s_brev_b32 s74, 8
	s_brev_b32 s75, 4
	v_mov_b32_e32 v139, 0xff800000
	v_readlane_b32 s76, v252, 10
	s_branch .LBB0_982
